# P5 K-loop mid hook (acc *= gb/ga) software-pipelined: 16 loads in flight with counted vmcnt instead of six load-wait-compute round trips
# speedup vs baseline: 1.0109x; 1.0047x over previous
;     DI void mid(f32x4 (&acc)[2][2][4][2], const pg8::Unit& u, int wr, int wc, int fr, int fq) const {
;         int fr_ = fr, fq_ = fq; asm volatile("" : "+v"(fr_), "+v"(fq_));
;         const int row0 = u.pm * 256 + wr * 64 + fr_, col0 = u.pn * 256 + wc * 32 + 8 * fq_;
; #pragma unroll
;         for (int ai = 0; ai < 2; ++ai)
; #pragma unroll
;             for (int m = 0; m < 4; ++m)
; #pragma unroll
;                 for (int bj = 0; bj < 2; ++bj) {
;                     const size_t o = (size_t)(row0 + ai * 128 + m * 16) * D + col0 + bj * 128;
;                     const u32x4 a = *(const u32x4*)(ga + o), b = *(const u32x4*)(gb + o);
;                     f32x4 r0, r1;
;                     r0[0] = bflo(b.x) * __builtin_amdgcn_rcpf(bflo(a.x)); r0[1] = bfhi(b.x) * __builtin_amdgcn_rcpf(bfhi(a.x)); r0[2] = bflo(b.y) * __builtin_amdgcn_rcpf(bflo(a.y)); r0[3] = bfhi(b.y) * __builtin_amdgcn_rcpf(bfhi(a.y));
;                     r1[0] = bflo(b.z) * __builtin_amdgcn_rcpf(bflo(a.z)); r1[1] = bfhi(b.z) * __builtin_amdgcn_rcpf(bfhi(a.z)); r1[2] = bflo(b.w) * __builtin_amdgcn_rcpf(bflo(a.w)); r1[3] = bfhi(b.w) * __builtin_amdgcn_rcpf(bfhi(a.w));
;                     acc[ai][bj][m][0] = acc[ai][bj][m][0] * r0; acc[ai][bj][m][1] = acc[ai][bj][m][1] * r1;
;                     if (bj == 1) asm volatile("" ::: "memory");
;                 }
;     }
.LBB0_602:
	s_cmpk_lg_i32 s50, 0x400
	s_cbranch_scc1 .LBB0_601
	v_mov_b32_e32 v3, v1
	v_mov_b32_e32 v132, v178
	v_add_u32_e32 v134, s81, v3
	v_lshl_add_u32 v132, v132, 3, s80
	v_ashrrev_i32_e32 v135, 31, v134
	v_ashrrev_i32_e32 v133, 31, v132
	v_lshlrev_b64 v[134:135], 11, v[134:135]
	v_lshl_add_u64 v[132:133], v[134:135], 0, v[132:133]
	v_lshlrev_b64 v[176:177], 1, v[132:133]
	v_lshl_add_u64 v[148:149], s[12:13], 0, v[176:177]
	global_load_dwordx4 v[184:187], v[148:149], off
	v_lshl_add_u64 v[150:151], s[14:15], 0, v[176:177]
	global_load_dwordx4 v[188:191], v[150:151], off
	global_load_dwordx4 v[192:195], v[148:149], off offset:256
	global_load_dwordx4 v[196:199], v[150:151], off offset:256
	v_lshl_add_u64 v[152:153], v[176:177], 0, s[22:23]
	v_lshl_add_u64 v[148:149], s[12:13], 0, v[152:153]
	global_load_dwordx4 v[200:203], v[148:149], off
	v_lshl_add_u64 v[150:151], s[14:15], 0, v[152:153]
	global_load_dwordx4 v[204:207], v[150:151], off
	global_load_dwordx4 v[208:211], v[148:149], off offset:256
	global_load_dwordx4 v[212:215], v[150:151], off offset:256
	v_lshl_add_u64 v[152:153], v[176:177], 0, s[24:25]
	v_lshl_add_u64 v[148:149], s[12:13], 0, v[152:153]
	global_load_dwordx4 v[216:219], v[148:149], off
	v_lshl_add_u64 v[150:151], s[14:15], 0, v[152:153]
	global_load_dwordx4 v[220:223], v[150:151], off
	global_load_dwordx4 v[224:227], v[148:149], off offset:256
	global_load_dwordx4 v[228:231], v[150:151], off offset:256
	v_lshl_add_u64 v[152:153], v[176:177], 0, s[26:27]
	v_lshl_add_u64 v[148:149], s[12:13], 0, v[152:153]
	global_load_dwordx4 v[132:135], v[148:149], off
	v_lshl_add_u64 v[150:151], s[14:15], 0, v[152:153]
	global_load_dwordx4 v[136:139], v[150:151], off
	global_load_dwordx4 v[140:143], v[148:149], off offset:256
	global_load_dwordx4 v[144:147], v[150:151], off offset:256
	s_waitcnt vmcnt(14)
	v_lshlrev_b32_e32 v152, 16, v184
	v_and_b32_e32 v153, 0xffff0000, v184
	v_rcp_f32_e32 v152, v152
	v_rcp_f32_e32 v153, v153
	v_lshlrev_b32_e32 v154, 16, v188
	v_and_b32_e32 v155, 0xffff0000, v188
	v_pk_mul_f32 v[152:153], v[152:153], v[154:155]
	v_pk_mul_f32 v[128:129], v[128:129], v[152:153]
	v_lshlrev_b32_e32 v152, 16, v185
	v_and_b32_e32 v153, 0xffff0000, v185
	v_rcp_f32_e32 v152, v152
	v_rcp_f32_e32 v153, v153
	v_lshlrev_b32_e32 v154, 16, v189
	v_and_b32_e32 v155, 0xffff0000, v189
	v_pk_mul_f32 v[152:153], v[152:153], v[154:155]
	v_pk_mul_f32 v[130:131], v[130:131], v[152:153]
	v_lshlrev_b32_e32 v152, 16, v186
	v_and_b32_e32 v153, 0xffff0000, v186
	v_rcp_f32_e32 v152, v152
	v_rcp_f32_e32 v153, v153
	v_lshlrev_b32_e32 v154, 16, v190
	v_and_b32_e32 v155, 0xffff0000, v190
	v_pk_mul_f32 v[152:153], v[152:153], v[154:155]
	v_pk_mul_f32 v[124:125], v[124:125], v[152:153]
	v_lshlrev_b32_e32 v152, 16, v187
	v_and_b32_e32 v153, 0xffff0000, v187
	v_rcp_f32_e32 v152, v152
	v_rcp_f32_e32 v153, v153
	v_lshlrev_b32_e32 v154, 16, v191
	v_and_b32_e32 v155, 0xffff0000, v191
	v_pk_mul_f32 v[152:153], v[152:153], v[154:155]
	v_pk_mul_f32 v[126:127], v[126:127], v[152:153]
	v_lshl_add_u64 v[152:153], v[176:177], 0, s[28:29]
	v_lshl_add_u64 v[148:149], s[12:13], 0, v[152:153]
	global_load_dwordx4 v[184:187], v[148:149], off
	v_lshl_add_u64 v[150:151], s[14:15], 0, v[152:153]
	global_load_dwordx4 v[188:191], v[150:151], off
	s_waitcnt vmcnt(14)
	v_lshlrev_b32_e32 v152, 16, v192
	v_and_b32_e32 v153, 0xffff0000, v192
	v_rcp_f32_e32 v152, v152
	v_rcp_f32_e32 v153, v153
	v_lshlrev_b32_e32 v154, 16, v196
	v_and_b32_e32 v155, 0xffff0000, v196
	v_pk_mul_f32 v[152:153], v[152:153], v[154:155]
	v_pk_mul_f32 v[120:121], v[120:121], v[152:153]
	v_lshlrev_b32_e32 v152, 16, v193
	v_and_b32_e32 v153, 0xffff0000, v193
	v_rcp_f32_e32 v152, v152
	v_rcp_f32_e32 v153, v153
	v_lshlrev_b32_e32 v154, 16, v197
	v_and_b32_e32 v155, 0xffff0000, v197
	v_pk_mul_f32 v[152:153], v[152:153], v[154:155]
	v_pk_mul_f32 v[122:123], v[122:123], v[152:153]
	v_lshlrev_b32_e32 v152, 16, v194
	v_and_b32_e32 v153, 0xffff0000, v194
	v_rcp_f32_e32 v152, v152
	v_rcp_f32_e32 v153, v153
	v_lshlrev_b32_e32 v154, 16, v198
	v_and_b32_e32 v155, 0xffff0000, v198
	v_pk_mul_f32 v[152:153], v[152:153], v[154:155]
	v_pk_mul_f32 v[116:117], v[116:117], v[152:153]
	v_lshlrev_b32_e32 v152, 16, v195
	v_and_b32_e32 v153, 0xffff0000, v195
	v_rcp_f32_e32 v152, v152
	v_rcp_f32_e32 v153, v153
	v_lshlrev_b32_e32 v154, 16, v199
	v_and_b32_e32 v155, 0xffff0000, v199
	v_pk_mul_f32 v[152:153], v[152:153], v[154:155]
	v_pk_mul_f32 v[118:119], v[118:119], v[152:153]
	v_lshl_add_u64 v[152:153], v[176:177], 0, s[28:29]
	v_lshl_add_u64 v[148:149], s[12:13], 0, v[152:153]
	global_load_dwordx4 v[192:195], v[148:149], off offset:256
	v_lshl_add_u64 v[150:151], s[14:15], 0, v[152:153]
	global_load_dwordx4 v[196:199], v[150:151], off offset:256
	s_waitcnt vmcnt(14)
	v_lshlrev_b32_e32 v152, 16, v200
	v_and_b32_e32 v153, 0xffff0000, v200
	v_rcp_f32_e32 v152, v152
	v_rcp_f32_e32 v153, v153
	v_lshlrev_b32_e32 v154, 16, v204
	v_and_b32_e32 v155, 0xffff0000, v204
	v_pk_mul_f32 v[152:153], v[152:153], v[154:155]
	v_pk_mul_f32 v[112:113], v[112:113], v[152:153]
	v_lshlrev_b32_e32 v152, 16, v201
	v_and_b32_e32 v153, 0xffff0000, v201
	v_rcp_f32_e32 v152, v152
	v_rcp_f32_e32 v153, v153
	v_lshlrev_b32_e32 v154, 16, v205
	v_and_b32_e32 v155, 0xffff0000, v205
	v_pk_mul_f32 v[152:153], v[152:153], v[154:155]
	v_pk_mul_f32 v[114:115], v[114:115], v[152:153]
	v_lshlrev_b32_e32 v152, 16, v202
	v_and_b32_e32 v153, 0xffff0000, v202
	v_rcp_f32_e32 v152, v152
	v_rcp_f32_e32 v153, v153
	v_lshlrev_b32_e32 v154, 16, v206
	v_and_b32_e32 v155, 0xffff0000, v206
	v_pk_mul_f32 v[152:153], v[152:153], v[154:155]
	v_pk_mul_f32 v[108:109], v[108:109], v[152:153]
	v_lshlrev_b32_e32 v152, 16, v203
	v_and_b32_e32 v153, 0xffff0000, v203
	v_rcp_f32_e32 v152, v152
	v_rcp_f32_e32 v153, v153
	v_lshlrev_b32_e32 v154, 16, v207
	v_and_b32_e32 v155, 0xffff0000, v207
	v_pk_mul_f32 v[152:153], v[152:153], v[154:155]
	v_pk_mul_f32 v[110:111], v[110:111], v[152:153]
	v_lshl_add_u64 v[152:153], v[176:177], 0, s[30:31]
	v_lshl_add_u64 v[148:149], s[12:13], 0, v[152:153]
	global_load_dwordx4 v[200:203], v[148:149], off
	v_lshl_add_u64 v[150:151], s[14:15], 0, v[152:153]
	global_load_dwordx4 v[204:207], v[150:151], off
	s_waitcnt vmcnt(14)
;     DI void mid(f32x4 (&acc)[2][2][4][2], const pg8::Unit& u, int wr, int wc, int fr, int fq) const {
;     ...
; #pragma unroll
;         for (int ai = 0; ai < 2; ++ai)
; #pragma unroll
;             for (int m = 0; m < 4; ++m)
; #pragma unroll
;                 for (int bj = 0; bj < 2; ++bj) {
;                     const size_t o = (size_t)(row0 + ai * 128 + m * 16) * D + col0 + bj * 128;
;                     const u32x4 a = *(const u32x4*)(ga + o), b = *(const u32x4*)(gb + o);
;                     f32x4 r0, r1;
;                     r0[0] = bflo(b.x) * __builtin_amdgcn_rcpf(bflo(a.x)); r0[1] = bfhi(b.x) * __builtin_amdgcn_rcpf(bfhi(a.x)); r0[2] = bflo(b.y) * __builtin_amdgcn_rcpf(bflo(a.y)); r0[3] = bfhi(b.y) * __builtin_amdgcn_rcpf(bfhi(a.y));
;                     r1[0] = bflo(b.z) * __builtin_amdgcn_rcpf(bflo(a.z)); r1[1] = bfhi(b.z) * __builtin_amdgcn_rcpf(bfhi(a.z)); r1[2] = bflo(b.w) * __builtin_amdgcn_rcpf(bflo(a.w)); r1[3] = bfhi(b.w) * __builtin_amdgcn_rcpf(bfhi(a.w));
;                     acc[ai][bj][m][0] = acc[ai][bj][m][0] * r0; acc[ai][bj][m][1] = acc[ai][bj][m][1] * r1;
;                     if (bj == 1) asm volatile("" ::: "memory");
;                 }
	v_lshlrev_b32_e32 v152, 16, v208
	v_and_b32_e32 v153, 0xffff0000, v208
	v_rcp_f32_e32 v152, v152
	v_rcp_f32_e32 v153, v153
	v_lshlrev_b32_e32 v154, 16, v212
	v_and_b32_e32 v155, 0xffff0000, v212
	v_pk_mul_f32 v[152:153], v[152:153], v[154:155]
	v_pk_mul_f32 v[104:105], v[104:105], v[152:153]
	v_lshlrev_b32_e32 v152, 16, v209
	v_and_b32_e32 v153, 0xffff0000, v209
	v_rcp_f32_e32 v152, v152
	v_rcp_f32_e32 v153, v153
	v_lshlrev_b32_e32 v154, 16, v213
	v_and_b32_e32 v155, 0xffff0000, v213
	v_pk_mul_f32 v[152:153], v[152:153], v[154:155]
	v_pk_mul_f32 v[106:107], v[106:107], v[152:153]
	v_lshlrev_b32_e32 v152, 16, v210
	v_and_b32_e32 v153, 0xffff0000, v210
	v_rcp_f32_e32 v152, v152
	v_rcp_f32_e32 v153, v153
	v_lshlrev_b32_e32 v154, 16, v214
	v_and_b32_e32 v155, 0xffff0000, v214
	v_pk_mul_f32 v[152:153], v[152:153], v[154:155]
	v_pk_mul_f32 v[100:101], v[100:101], v[152:153]
	v_lshlrev_b32_e32 v152, 16, v211
	v_and_b32_e32 v153, 0xffff0000, v211
	v_rcp_f32_e32 v152, v152
	v_rcp_f32_e32 v153, v153
	v_lshlrev_b32_e32 v154, 16, v215
	v_and_b32_e32 v155, 0xffff0000, v215
	v_pk_mul_f32 v[152:153], v[152:153], v[154:155]
	v_pk_mul_f32 v[102:103], v[102:103], v[152:153]
	v_lshl_add_u64 v[152:153], v[176:177], 0, s[30:31]
	v_lshl_add_u64 v[148:149], s[12:13], 0, v[152:153]
	global_load_dwordx4 v[208:211], v[148:149], off offset:256
	v_lshl_add_u64 v[150:151], s[14:15], 0, v[152:153]
	global_load_dwordx4 v[212:215], v[150:151], off offset:256
	s_waitcnt vmcnt(14)
	v_lshlrev_b32_e32 v152, 16, v216
	v_and_b32_e32 v153, 0xffff0000, v216
	v_rcp_f32_e32 v152, v152
	v_rcp_f32_e32 v153, v153
	v_lshlrev_b32_e32 v154, 16, v220
	v_and_b32_e32 v155, 0xffff0000, v220
	v_pk_mul_f32 v[152:153], v[152:153], v[154:155]
	v_pk_mul_f32 v[96:97], v[96:97], v[152:153]
	v_lshlrev_b32_e32 v152, 16, v217
	v_and_b32_e32 v153, 0xffff0000, v217
	v_rcp_f32_e32 v152, v152
	v_rcp_f32_e32 v153, v153
	v_lshlrev_b32_e32 v154, 16, v221
	v_and_b32_e32 v155, 0xffff0000, v221
	v_pk_mul_f32 v[152:153], v[152:153], v[154:155]
	v_pk_mul_f32 v[98:99], v[98:99], v[152:153]
	v_lshlrev_b32_e32 v152, 16, v218
	v_and_b32_e32 v153, 0xffff0000, v218
	v_rcp_f32_e32 v152, v152
	v_rcp_f32_e32 v153, v153
	v_lshlrev_b32_e32 v154, 16, v222
	v_and_b32_e32 v155, 0xffff0000, v222
	v_pk_mul_f32 v[152:153], v[152:153], v[154:155]
	v_pk_mul_f32 v[92:93], v[92:93], v[152:153]
	v_lshlrev_b32_e32 v152, 16, v219
	v_and_b32_e32 v153, 0xffff0000, v219
	v_rcp_f32_e32 v152, v152
	v_rcp_f32_e32 v153, v153
	v_lshlrev_b32_e32 v154, 16, v223
	v_and_b32_e32 v155, 0xffff0000, v223
	v_pk_mul_f32 v[152:153], v[152:153], v[154:155]
	v_pk_mul_f32 v[94:95], v[94:95], v[152:153]
	v_lshl_add_u64 v[152:153], v[176:177], 0, s[8:9]
	v_lshl_add_u64 v[148:149], s[12:13], 0, v[152:153]
	global_load_dwordx4 v[216:219], v[148:149], off
	v_lshl_add_u64 v[150:151], s[14:15], 0, v[152:153]
	global_load_dwordx4 v[220:223], v[150:151], off
	s_waitcnt vmcnt(14)
	v_lshlrev_b32_e32 v152, 16, v224
	v_and_b32_e32 v153, 0xffff0000, v224
	v_rcp_f32_e32 v152, v152
	v_rcp_f32_e32 v153, v153
	v_lshlrev_b32_e32 v154, 16, v228
	v_and_b32_e32 v155, 0xffff0000, v228
	v_pk_mul_f32 v[152:153], v[152:153], v[154:155]
	v_pk_mul_f32 v[88:89], v[88:89], v[152:153]
	v_lshlrev_b32_e32 v152, 16, v225
	v_and_b32_e32 v153, 0xffff0000, v225
	v_rcp_f32_e32 v152, v152
	v_rcp_f32_e32 v153, v153
	v_lshlrev_b32_e32 v154, 16, v229
	v_and_b32_e32 v155, 0xffff0000, v229
	v_pk_mul_f32 v[152:153], v[152:153], v[154:155]
	v_pk_mul_f32 v[90:91], v[90:91], v[152:153]
	v_lshlrev_b32_e32 v152, 16, v226
	v_and_b32_e32 v153, 0xffff0000, v226
	v_rcp_f32_e32 v152, v152
	v_rcp_f32_e32 v153, v153
	v_lshlrev_b32_e32 v154, 16, v230
	v_and_b32_e32 v155, 0xffff0000, v230
	v_pk_mul_f32 v[152:153], v[152:153], v[154:155]
	v_pk_mul_f32 v[84:85], v[84:85], v[152:153]
	v_lshlrev_b32_e32 v152, 16, v227
	v_and_b32_e32 v153, 0xffff0000, v227
	v_rcp_f32_e32 v152, v152
	v_rcp_f32_e32 v153, v153
	v_lshlrev_b32_e32 v154, 16, v231
	v_and_b32_e32 v155, 0xffff0000, v231
	v_pk_mul_f32 v[152:153], v[152:153], v[154:155]
	v_pk_mul_f32 v[86:87], v[86:87], v[152:153]
	v_lshl_add_u64 v[152:153], v[176:177], 0, s[8:9]
	v_lshl_add_u64 v[148:149], s[12:13], 0, v[152:153]
	global_load_dwordx4 v[224:227], v[148:149], off offset:256
	v_lshl_add_u64 v[150:151], s[14:15], 0, v[152:153]
	global_load_dwordx4 v[228:231], v[150:151], off offset:256
	s_waitcnt vmcnt(14)
	v_lshlrev_b32_e32 v152, 16, v132
	v_and_b32_e32 v153, 0xffff0000, v132
	v_rcp_f32_e32 v152, v152
	v_rcp_f32_e32 v153, v153
	v_lshlrev_b32_e32 v154, 16, v136
	v_and_b32_e32 v155, 0xffff0000, v136
	v_pk_mul_f32 v[152:153], v[152:153], v[154:155]
	v_pk_mul_f32 v[80:81], v[80:81], v[152:153]
	v_lshlrev_b32_e32 v152, 16, v133
	v_and_b32_e32 v153, 0xffff0000, v133
	v_rcp_f32_e32 v152, v152
	v_rcp_f32_e32 v153, v153
	v_lshlrev_b32_e32 v154, 16, v137
	v_and_b32_e32 v155, 0xffff0000, v137
	v_pk_mul_f32 v[152:153], v[152:153], v[154:155]
	v_pk_mul_f32 v[82:83], v[82:83], v[152:153]
	v_lshlrev_b32_e32 v152, 16, v134
	v_and_b32_e32 v153, 0xffff0000, v134
	v_rcp_f32_e32 v152, v152
	v_rcp_f32_e32 v153, v153
	v_lshlrev_b32_e32 v154, 16, v138
	v_and_b32_e32 v155, 0xffff0000, v138
	v_pk_mul_f32 v[152:153], v[152:153], v[154:155]
	v_pk_mul_f32 v[76:77], v[76:77], v[152:153]
	v_lshlrev_b32_e32 v152, 16, v135
	v_and_b32_e32 v153, 0xffff0000, v135
	v_rcp_f32_e32 v152, v152
	v_rcp_f32_e32 v153, v153
	v_lshlrev_b32_e32 v154, 16, v139
	v_and_b32_e32 v155, 0xffff0000, v139
	v_pk_mul_f32 v[152:153], v[152:153], v[154:155]
	v_pk_mul_f32 v[78:79], v[78:79], v[152:153]
	v_lshl_add_u64 v[152:153], v[176:177], 0, s[34:35]
	v_lshl_add_u64 v[148:149], s[12:13], 0, v[152:153]
	global_load_dwordx4 v[132:135], v[148:149], off
	v_lshl_add_u64 v[150:151], s[14:15], 0, v[152:153]
	global_load_dwordx4 v[136:139], v[150:151], off
	s_waitcnt vmcnt(14)
;     DI void mid(f32x4 (&acc)[2][2][4][2], const pg8::Unit& u, int wr, int wc, int fr, int fq) const {
;     ...
; #pragma unroll
;         for (int ai = 0; ai < 2; ++ai)
; #pragma unroll
;             for (int m = 0; m < 4; ++m)
; #pragma unroll
;                 for (int bj = 0; bj < 2; ++bj) {
;                     const size_t o = (size_t)(row0 + ai * 128 + m * 16) * D + col0 + bj * 128;
;                     const u32x4 a = *(const u32x4*)(ga + o), b = *(const u32x4*)(gb + o);
;                     f32x4 r0, r1;
;                     r0[0] = bflo(b.x) * __builtin_amdgcn_rcpf(bflo(a.x)); r0[1] = bfhi(b.x) * __builtin_amdgcn_rcpf(bfhi(a.x)); r0[2] = bflo(b.y) * __builtin_amdgcn_rcpf(bflo(a.y)); r0[3] = bfhi(b.y) * __builtin_amdgcn_rcpf(bfhi(a.y));
;                     r1[0] = bflo(b.z) * __builtin_amdgcn_rcpf(bflo(a.z)); r1[1] = bfhi(b.z) * __builtin_amdgcn_rcpf(bfhi(a.z)); r1[2] = bflo(b.w) * __builtin_amdgcn_rcpf(bflo(a.w)); r1[3] = bfhi(b.w) * __builtin_amdgcn_rcpf(bfhi(a.w));
;                     acc[ai][bj][m][0] = acc[ai][bj][m][0] * r0; acc[ai][bj][m][1] = acc[ai][bj][m][1] * r1;
;                     if (bj == 1) asm volatile("" ::: "memory");
;                 }
	v_lshlrev_b32_e32 v152, 16, v140
	v_and_b32_e32 v153, 0xffff0000, v140
	v_rcp_f32_e32 v152, v152
	v_rcp_f32_e32 v153, v153
	v_lshlrev_b32_e32 v154, 16, v144
	v_and_b32_e32 v155, 0xffff0000, v144
	v_pk_mul_f32 v[152:153], v[152:153], v[154:155]
	v_pk_mul_f32 v[72:73], v[72:73], v[152:153]
	v_lshlrev_b32_e32 v152, 16, v141
	v_and_b32_e32 v153, 0xffff0000, v141
	v_rcp_f32_e32 v152, v152
	v_rcp_f32_e32 v153, v153
	v_lshlrev_b32_e32 v154, 16, v145
	v_and_b32_e32 v155, 0xffff0000, v145
	v_pk_mul_f32 v[152:153], v[152:153], v[154:155]
	v_pk_mul_f32 v[74:75], v[74:75], v[152:153]
	v_lshlrev_b32_e32 v152, 16, v142
	v_and_b32_e32 v153, 0xffff0000, v142
	v_rcp_f32_e32 v152, v152
	v_rcp_f32_e32 v153, v153
	v_lshlrev_b32_e32 v154, 16, v146
	v_and_b32_e32 v155, 0xffff0000, v146
	v_pk_mul_f32 v[152:153], v[152:153], v[154:155]
	v_pk_mul_f32 v[68:69], v[68:69], v[152:153]
	v_lshlrev_b32_e32 v152, 16, v143
	v_and_b32_e32 v153, 0xffff0000, v143
	v_rcp_f32_e32 v152, v152
	v_rcp_f32_e32 v153, v153
	v_lshlrev_b32_e32 v154, 16, v147
	v_and_b32_e32 v155, 0xffff0000, v147
	v_pk_mul_f32 v[152:153], v[152:153], v[154:155]
	v_pk_mul_f32 v[70:71], v[70:71], v[152:153]
	v_lshl_add_u64 v[152:153], v[176:177], 0, s[34:35]
	v_lshl_add_u64 v[148:149], s[12:13], 0, v[152:153]
	global_load_dwordx4 v[140:143], v[148:149], off offset:256
	v_lshl_add_u64 v[150:151], s[14:15], 0, v[152:153]
	global_load_dwordx4 v[144:147], v[150:151], off offset:256
	s_waitcnt vmcnt(14)
	v_lshlrev_b32_e32 v152, 16, v184
	v_and_b32_e32 v153, 0xffff0000, v184
	v_rcp_f32_e32 v152, v152
	v_rcp_f32_e32 v153, v153
	v_lshlrev_b32_e32 v154, 16, v188
	v_and_b32_e32 v155, 0xffff0000, v188
	v_pk_mul_f32 v[152:153], v[152:153], v[154:155]
	v_pk_mul_f32 v[64:65], v[64:65], v[152:153]
	v_lshlrev_b32_e32 v152, 16, v185
	v_and_b32_e32 v153, 0xffff0000, v185
	v_rcp_f32_e32 v152, v152
	v_rcp_f32_e32 v153, v153
	v_lshlrev_b32_e32 v154, 16, v189
	v_and_b32_e32 v155, 0xffff0000, v189
	v_pk_mul_f32 v[152:153], v[152:153], v[154:155]
	v_pk_mul_f32 v[66:67], v[66:67], v[152:153]
	v_lshlrev_b32_e32 v152, 16, v186
	v_and_b32_e32 v153, 0xffff0000, v186
	v_rcp_f32_e32 v152, v152
	v_rcp_f32_e32 v153, v153
	v_lshlrev_b32_e32 v154, 16, v190
	v_and_b32_e32 v155, 0xffff0000, v190
	v_pk_mul_f32 v[152:153], v[152:153], v[154:155]
	v_pk_mul_f32 v[60:61], v[60:61], v[152:153]
	v_lshlrev_b32_e32 v152, 16, v187
	v_and_b32_e32 v153, 0xffff0000, v187
	v_rcp_f32_e32 v152, v152
	v_rcp_f32_e32 v153, v153
	v_lshlrev_b32_e32 v154, 16, v191
	v_and_b32_e32 v155, 0xffff0000, v191
	v_pk_mul_f32 v[152:153], v[152:153], v[154:155]
	v_pk_mul_f32 v[62:63], v[62:63], v[152:153]
	s_waitcnt vmcnt(12)
	v_lshlrev_b32_e32 v152, 16, v192
	v_and_b32_e32 v153, 0xffff0000, v192
	v_rcp_f32_e32 v152, v152
	v_rcp_f32_e32 v153, v153
	v_lshlrev_b32_e32 v154, 16, v196
	v_and_b32_e32 v155, 0xffff0000, v196
	v_pk_mul_f32 v[152:153], v[152:153], v[154:155]
	v_pk_mul_f32 v[56:57], v[56:57], v[152:153]
	v_lshlrev_b32_e32 v152, 16, v193
	v_and_b32_e32 v153, 0xffff0000, v193
	v_rcp_f32_e32 v152, v152
	v_rcp_f32_e32 v153, v153
	v_lshlrev_b32_e32 v154, 16, v197
	v_and_b32_e32 v155, 0xffff0000, v197
	v_pk_mul_f32 v[152:153], v[152:153], v[154:155]
	v_pk_mul_f32 v[58:59], v[58:59], v[152:153]
	v_lshlrev_b32_e32 v152, 16, v194
	v_and_b32_e32 v153, 0xffff0000, v194
	v_rcp_f32_e32 v152, v152
	v_rcp_f32_e32 v153, v153
	v_lshlrev_b32_e32 v154, 16, v198
	v_and_b32_e32 v155, 0xffff0000, v198
	v_pk_mul_f32 v[152:153], v[152:153], v[154:155]
	v_pk_mul_f32 v[52:53], v[52:53], v[152:153]
	v_lshlrev_b32_e32 v152, 16, v195
	v_and_b32_e32 v153, 0xffff0000, v195
	v_rcp_f32_e32 v152, v152
	v_rcp_f32_e32 v153, v153
	v_lshlrev_b32_e32 v154, 16, v199
	v_and_b32_e32 v155, 0xffff0000, v199
	v_pk_mul_f32 v[152:153], v[152:153], v[154:155]
	v_pk_mul_f32 v[54:55], v[54:55], v[152:153]
	s_waitcnt vmcnt(10)
	v_lshlrev_b32_e32 v152, 16, v200
	v_and_b32_e32 v153, 0xffff0000, v200
	v_rcp_f32_e32 v152, v152
	v_rcp_f32_e32 v153, v153
	v_lshlrev_b32_e32 v154, 16, v204
	v_and_b32_e32 v155, 0xffff0000, v204
	v_pk_mul_f32 v[152:153], v[152:153], v[154:155]
	v_pk_mul_f32 v[48:49], v[48:49], v[152:153]
	v_lshlrev_b32_e32 v152, 16, v201
	v_and_b32_e32 v153, 0xffff0000, v201
	v_rcp_f32_e32 v152, v152
	v_rcp_f32_e32 v153, v153
	v_lshlrev_b32_e32 v154, 16, v205
	v_and_b32_e32 v155, 0xffff0000, v205
	v_pk_mul_f32 v[152:153], v[152:153], v[154:155]
	v_pk_mul_f32 v[50:51], v[50:51], v[152:153]
	v_lshlrev_b32_e32 v152, 16, v202
	v_and_b32_e32 v153, 0xffff0000, v202
	v_rcp_f32_e32 v152, v152
	v_rcp_f32_e32 v153, v153
	v_lshlrev_b32_e32 v154, 16, v206
	v_and_b32_e32 v155, 0xffff0000, v206
	v_pk_mul_f32 v[152:153], v[152:153], v[154:155]
	v_pk_mul_f32 v[44:45], v[44:45], v[152:153]
	v_lshlrev_b32_e32 v152, 16, v203
	v_and_b32_e32 v153, 0xffff0000, v203
	v_rcp_f32_e32 v152, v152
	v_rcp_f32_e32 v153, v153
	v_lshlrev_b32_e32 v154, 16, v207
	v_and_b32_e32 v155, 0xffff0000, v207
	v_pk_mul_f32 v[152:153], v[152:153], v[154:155]
	v_pk_mul_f32 v[46:47], v[46:47], v[152:153]
	s_waitcnt vmcnt(8)
;     DI void mid(f32x4 (&acc)[2][2][4][2], const pg8::Unit& u, int wr, int wc, int fr, int fq) const {
;     ...
; #pragma unroll
;         for (int ai = 0; ai < 2; ++ai)
; #pragma unroll
;             for (int m = 0; m < 4; ++m)
; #pragma unroll
;                 for (int bj = 0; bj < 2; ++bj) {
;                     const size_t o = (size_t)(row0 + ai * 128 + m * 16) * D + col0 + bj * 128;
;                     const u32x4 a = *(const u32x4*)(ga + o), b = *(const u32x4*)(gb + o);
;                     f32x4 r0, r1;
;                     r0[0] = bflo(b.x) * __builtin_amdgcn_rcpf(bflo(a.x)); r0[1] = bfhi(b.x) * __builtin_amdgcn_rcpf(bfhi(a.x)); r0[2] = bflo(b.y) * __builtin_amdgcn_rcpf(bflo(a.y)); r0[3] = bfhi(b.y) * __builtin_amdgcn_rcpf(bfhi(a.y));
;                     r1[0] = bflo(b.z) * __builtin_amdgcn_rcpf(bflo(a.z)); r1[1] = bfhi(b.z) * __builtin_amdgcn_rcpf(bfhi(a.z)); r1[2] = bflo(b.w) * __builtin_amdgcn_rcpf(bflo(a.w)); r1[3] = bfhi(b.w) * __builtin_amdgcn_rcpf(bfhi(a.w));
;                     acc[ai][bj][m][0] = acc[ai][bj][m][0] * r0; acc[ai][bj][m][1] = acc[ai][bj][m][1] * r1;
;                     if (bj == 1) asm volatile("" ::: "memory");
;                 }
	v_lshlrev_b32_e32 v152, 16, v208
	v_and_b32_e32 v153, 0xffff0000, v208
	v_rcp_f32_e32 v152, v152
	v_rcp_f32_e32 v153, v153
	v_lshlrev_b32_e32 v154, 16, v212
	v_and_b32_e32 v155, 0xffff0000, v212
	v_pk_mul_f32 v[152:153], v[152:153], v[154:155]
	v_pk_mul_f32 v[40:41], v[40:41], v[152:153]
	v_lshlrev_b32_e32 v152, 16, v209
	v_and_b32_e32 v153, 0xffff0000, v209
	v_rcp_f32_e32 v152, v152
	v_rcp_f32_e32 v153, v153
	v_lshlrev_b32_e32 v154, 16, v213
	v_and_b32_e32 v155, 0xffff0000, v213
	v_pk_mul_f32 v[152:153], v[152:153], v[154:155]
	v_pk_mul_f32 v[42:43], v[42:43], v[152:153]
	v_lshlrev_b32_e32 v152, 16, v210
	v_and_b32_e32 v153, 0xffff0000, v210
	v_rcp_f32_e32 v152, v152
	v_rcp_f32_e32 v153, v153
	v_lshlrev_b32_e32 v154, 16, v214
	v_and_b32_e32 v155, 0xffff0000, v214
	v_pk_mul_f32 v[152:153], v[152:153], v[154:155]
	v_pk_mul_f32 v[36:37], v[36:37], v[152:153]
	v_lshlrev_b32_e32 v152, 16, v211
	v_and_b32_e32 v153, 0xffff0000, v211
	v_rcp_f32_e32 v152, v152
	v_rcp_f32_e32 v153, v153
	v_lshlrev_b32_e32 v154, 16, v215
	v_and_b32_e32 v155, 0xffff0000, v215
	v_pk_mul_f32 v[152:153], v[152:153], v[154:155]
	v_pk_mul_f32 v[38:39], v[38:39], v[152:153]
	s_waitcnt vmcnt(6)
	v_lshlrev_b32_e32 v152, 16, v216
	v_and_b32_e32 v153, 0xffff0000, v216
	v_rcp_f32_e32 v152, v152
	v_rcp_f32_e32 v153, v153
	v_lshlrev_b32_e32 v154, 16, v220
	v_and_b32_e32 v155, 0xffff0000, v220
	v_pk_mul_f32 v[152:153], v[152:153], v[154:155]
	v_pk_mul_f32 v[32:33], v[32:33], v[152:153]
	v_lshlrev_b32_e32 v152, 16, v217
	v_and_b32_e32 v153, 0xffff0000, v217
	v_rcp_f32_e32 v152, v152
	v_rcp_f32_e32 v153, v153
	v_lshlrev_b32_e32 v154, 16, v221
	v_and_b32_e32 v155, 0xffff0000, v221
	v_pk_mul_f32 v[152:153], v[152:153], v[154:155]
	v_pk_mul_f32 v[34:35], v[34:35], v[152:153]
	v_lshlrev_b32_e32 v152, 16, v218
	v_and_b32_e32 v153, 0xffff0000, v218
	v_rcp_f32_e32 v152, v152
	v_rcp_f32_e32 v153, v153
	v_lshlrev_b32_e32 v154, 16, v222
	v_and_b32_e32 v155, 0xffff0000, v222
	v_pk_mul_f32 v[152:153], v[152:153], v[154:155]
	v_pk_mul_f32 v[28:29], v[28:29], v[152:153]
	v_lshlrev_b32_e32 v152, 16, v219
	v_and_b32_e32 v153, 0xffff0000, v219
	v_rcp_f32_e32 v152, v152
	v_rcp_f32_e32 v153, v153
	v_lshlrev_b32_e32 v154, 16, v223
	v_and_b32_e32 v155, 0xffff0000, v223
	v_pk_mul_f32 v[152:153], v[152:153], v[154:155]
	v_pk_mul_f32 v[30:31], v[30:31], v[152:153]
	s_waitcnt vmcnt(4)
	v_lshlrev_b32_e32 v152, 16, v224
	v_and_b32_e32 v153, 0xffff0000, v224
	v_rcp_f32_e32 v152, v152
	v_rcp_f32_e32 v153, v153
	v_lshlrev_b32_e32 v154, 16, v228
	v_and_b32_e32 v155, 0xffff0000, v228
	v_pk_mul_f32 v[152:153], v[152:153], v[154:155]
	v_pk_mul_f32 v[24:25], v[24:25], v[152:153]
	v_lshlrev_b32_e32 v152, 16, v225
	v_and_b32_e32 v153, 0xffff0000, v225
	v_rcp_f32_e32 v152, v152
	v_rcp_f32_e32 v153, v153
	v_lshlrev_b32_e32 v154, 16, v229
	v_and_b32_e32 v155, 0xffff0000, v229
	v_pk_mul_f32 v[152:153], v[152:153], v[154:155]
	v_pk_mul_f32 v[26:27], v[26:27], v[152:153]
	v_lshlrev_b32_e32 v152, 16, v226
	v_and_b32_e32 v153, 0xffff0000, v226
	v_rcp_f32_e32 v152, v152
	v_rcp_f32_e32 v153, v153
	v_lshlrev_b32_e32 v154, 16, v230
	v_and_b32_e32 v155, 0xffff0000, v230
	v_pk_mul_f32 v[152:153], v[152:153], v[154:155]
	v_pk_mul_f32 v[20:21], v[20:21], v[152:153]
	v_lshlrev_b32_e32 v152, 16, v227
	v_and_b32_e32 v153, 0xffff0000, v227
	v_rcp_f32_e32 v152, v152
	v_rcp_f32_e32 v153, v153
	v_lshlrev_b32_e32 v154, 16, v231
	v_and_b32_e32 v155, 0xffff0000, v231
	v_pk_mul_f32 v[152:153], v[152:153], v[154:155]
	v_pk_mul_f32 v[22:23], v[22:23], v[152:153]
	s_waitcnt vmcnt(2)
	v_lshlrev_b32_e32 v152, 16, v132
	v_and_b32_e32 v153, 0xffff0000, v132
	v_rcp_f32_e32 v152, v152
	v_rcp_f32_e32 v153, v153
	v_lshlrev_b32_e32 v154, 16, v136
	v_and_b32_e32 v155, 0xffff0000, v136
	v_pk_mul_f32 v[152:153], v[152:153], v[154:155]
	v_pk_mul_f32 v[16:17], v[16:17], v[152:153]
	v_lshlrev_b32_e32 v152, 16, v133
	v_and_b32_e32 v153, 0xffff0000, v133
	v_rcp_f32_e32 v152, v152
	v_rcp_f32_e32 v153, v153
	v_lshlrev_b32_e32 v154, 16, v137
	v_and_b32_e32 v155, 0xffff0000, v137
	v_pk_mul_f32 v[152:153], v[152:153], v[154:155]
	v_pk_mul_f32 v[18:19], v[18:19], v[152:153]
	v_lshlrev_b32_e32 v152, 16, v134
	v_and_b32_e32 v153, 0xffff0000, v134
	v_rcp_f32_e32 v152, v152
	v_rcp_f32_e32 v153, v153
	v_lshlrev_b32_e32 v154, 16, v138
	v_and_b32_e32 v155, 0xffff0000, v138
	v_pk_mul_f32 v[152:153], v[152:153], v[154:155]
	v_pk_mul_f32 v[12:13], v[12:13], v[152:153]
	v_lshlrev_b32_e32 v152, 16, v135
	v_and_b32_e32 v153, 0xffff0000, v135
	v_rcp_f32_e32 v152, v152
	v_rcp_f32_e32 v153, v153
	v_lshlrev_b32_e32 v154, 16, v139
	v_and_b32_e32 v155, 0xffff0000, v139
	v_pk_mul_f32 v[152:153], v[152:153], v[154:155]
	v_pk_mul_f32 v[14:15], v[14:15], v[152:153]
	s_waitcnt vmcnt(0)
	v_lshlrev_b32_e32 v152, 16, v140
	v_and_b32_e32 v153, 0xffff0000, v140
	v_rcp_f32_e32 v152, v152
	v_rcp_f32_e32 v153, v153
	v_lshlrev_b32_e32 v154, 16, v144
	v_and_b32_e32 v155, 0xffff0000, v144
	v_pk_mul_f32 v[152:153], v[152:153], v[154:155]
	v_pk_mul_f32 v[8:9], v[8:9], v[152:153]
	v_lshlrev_b32_e32 v152, 16, v141
	v_and_b32_e32 v153, 0xffff0000, v141
	v_rcp_f32_e32 v152, v152
	v_rcp_f32_e32 v153, v153
	v_lshlrev_b32_e32 v154, 16, v145
	v_and_b32_e32 v155, 0xffff0000, v145
	v_pk_mul_f32 v[152:153], v[152:153], v[154:155]
	v_pk_mul_f32 v[10:11], v[10:11], v[152:153]
	v_lshlrev_b32_e32 v152, 16, v142
	v_and_b32_e32 v153, 0xffff0000, v142
	v_rcp_f32_e32 v152, v152
	v_rcp_f32_e32 v153, v153
	v_lshlrev_b32_e32 v154, 16, v146
	v_and_b32_e32 v155, 0xffff0000, v146
	v_pk_mul_f32 v[152:153], v[152:153], v[154:155]
	v_pk_mul_f32 v[4:5], v[4:5], v[152:153]
	v_lshlrev_b32_e32 v152, 16, v143
	v_and_b32_e32 v153, 0xffff0000, v143
	v_rcp_f32_e32 v152, v152
	v_rcp_f32_e32 v153, v153
	v_lshlrev_b32_e32 v154, 16, v147
	v_and_b32_e32 v155, 0xffff0000, v147
	v_pk_mul_f32 v[152:153], v[152:153], v[154:155]
	v_pk_mul_f32 v[6:7], v[6:7], v[152:153]
	s_branch .LBB0_601
